# v39 + norm phases P6 and P9: gain/shift/scale pieces of steps 1..7 loaded at the row top; per-step store->loads->vmcnt(2,1,0) chain (seven output-store drains per row) removed
# speedup vs baseline: 1.0125x; 1.0031x over previous
; #define GAS __attribute__((address_space(1)))
; template <bool F8, bool SRCH = false> __device__ __forceinline__ void norm_phase(Frame& F, const float* srcL, const float* srcC, const float* g, const float* mod, int shift_off, int scale_off, int nrows) {
;     ...
;     for (int row = gw; row < nrows; row += NGW) {
;         const float* src = row < ML ? srcL + (size_t)row * DM : srcC + (size_t)(row - ML) * DM;
;         const float* mv = mod + (size_t)(row < ML ? (row >> 13) : 2) * MOD_W;
;         const GAS f32x4* xr = (const GAS f32x4*)src + F.lane;
;         f32x4 v[8]; float s = 0.f;
; #pragma unroll
;         for (int j = 0; j < 8; ++j) {
;             if constexpr (SRCH) { const v2u w = ((const GAS v2u*)(WSP(const bf16, WS_H) + (size_t)row * DM))[F.lane + 64 * j]; v[j].x = bflo(w.x); v[j].y = bfhi(w.x); v[j].z = bflo(w.y); v[j].w = bfhi(w.y); }
;             else v[j] = xr[64 * j];
;             s += (v[j].x * v[j].x + v[j].y * v[j].y) + (v[j].z * v[j].z + v[j].w * v[j].w); }
;         const float rstd = 1.0f / sqrtf(wave_sum(s) * (1.0f / DM) + NORM_EPS);
.LBB0_603:
	v_lshl_add_u64 v[24:25], s[88:89], 0, v[20:21]
	v_add_co_u32_e32 v24, vcc, 0x4d800000, v24
	global_load_dwordx4 v[58:61], v[2:3], off
	s_nop 0
	v_addc_co_u32_e32 v25, vcc, 0, v25, vcc
	global_load_dwordx2 v[26:27], v[24:25], off
	global_load_dwordx2 v[28:29], v[24:25], off offset:512
	global_load_dwordx2 v[30:31], v[24:25], off offset:1024
	global_load_dwordx2 v[32:33], v[24:25], off offset:1536
	global_load_dwordx2 v[34:35], v[24:25], off offset:2048
	global_load_dwordx2 v[36:37], v[24:25], off offset:2560
	global_load_dwordx2 v[70:71], v[24:25], off offset:3072
	global_load_dwordx2 v[72:73], v[24:25], off offset:3584
	s_min_i32 s0, s4, 0x4000
	v_lshl_add_u64 v[22:23], s[88:89], 0, v[18:19]
	s_ashr_i32 s12, s0, 13
	v_add_co_u32_e64 v22, s[0:1], s18, v22
	v_mov_b32_e32 v110, 0
	s_nop 0
	v_addc_co_u32_e64 v23, s[0:1], 0, v23, s[0:1]
	s_mul_hi_i32 s0, s12, 0xc000
	s_mul_i32 s12, s12, 0xc000
	s_add_u32 s1, s16, s12
	s_addc_u32 s0, s17, s0
	s_add_u32 s12, s1, 0x6000
	s_addc_u32 s13, s0, 0
	s_add_u32 s14, s1, 0x8000
	s_addc_u32 s15, s0, 0
	global_load_dwordx4 v[62:65], v49, s[12:13]
	global_load_dwordx4 v[66:69], v49, s[14:15]
	global_load_dwordx4 v[118:121], v[4:5], off
	global_load_dwordx4 v[122:125], v50, s[14:15]
	global_load_dwordx4 v[126:129], v50, s[12:13]
	global_load_dwordx4 v[130:133], v[6:7], off
	global_load_dwordx4 v[134:137], v51, s[14:15]
	global_load_dwordx4 v[138:141], v51, s[12:13]
	global_load_dwordx4 v[142:145], v[8:9], off
	global_load_dwordx4 v[146:149], v52, s[14:15]
	global_load_dwordx4 v[150:153], v52, s[12:13]
	global_load_dwordx4 v[154:157], v[10:11], off
	global_load_dwordx4 v[158:161], v53, s[14:15]
	global_load_dwordx4 v[162:165], v53, s[12:13]
	global_load_dwordx4 v[166:169], v[12:13], off
	global_load_dwordx4 v[170:173], v54, s[14:15]
	global_load_dwordx4 v[174:177], v54, s[12:13]
	global_load_dwordx4 v[182:185], v[14:15], off
	global_load_dwordx4 v[186:189], v55, s[14:15]
	global_load_dwordx4 v[190:193], v55, s[12:13]
	global_load_dwordx4 v[194:197], v[16:17], off
	global_load_dwordx4 v[198:201], v56, s[14:15]
	global_load_dwordx4 v[202:205], v56, s[12:13]
	s_add_i32 s4, s4, s6
	v_lshl_add_u64 v[18:19], v[18:19], 0, s[8:9]
	v_lshl_add_u64 v[20:21], v[20:21], 0, s[10:11]
	s_cmpk_lt_i32 s4, 0x4200
	s_waitcnt vmcnt(30)
	v_and_b32_e32 v75, 0xffff0000, v26
	v_and_b32_e32 v77, 0xffff0000, v27
	v_lshlrev_b32_e32 v74, 16, v26
	v_lshlrev_b32_e32 v76, 16, v27
	s_waitcnt vmcnt(29)
	v_and_b32_e32 v81, 0xffff0000, v29
	v_and_b32_e32 v80, 0xffff0000, v28
	s_waitcnt vmcnt(28)
	v_and_b32_e32 v83, 0xffff0000, v30
	v_and_b32_e32 v85, 0xffff0000, v31
	s_waitcnt vmcnt(27)
	v_lshlrev_b32_e32 v87, 16, v32
	s_waitcnt vmcnt(23)
	v_lshlrev_b32_e32 v27, 16, v72
	v_and_b32_e32 v25, 0xffff0000, v72
	v_mul_f32_e32 v24, v77, v77
	v_mul_f32_e32 v26, v75, v75
	v_lshlrev_b32_e32 v79, 16, v29
	v_lshlrev_b32_e32 v78, 16, v28
	v_lshlrev_b32_e32 v82, 16, v30
	v_lshlrev_b32_e32 v84, 16, v31
	v_and_b32_e32 v89, 0xffff0000, v32
	v_lshlrev_b32_e32 v90, 16, v33
	v_and_b32_e32 v91, 0xffff0000, v33
	v_lshlrev_b32_e32 v30, 16, v70
	v_and_b32_e32 v31, 0xffff0000, v70
	v_lshlrev_b32_e32 v32, 16, v71
	v_and_b32_e32 v33, 0xffff0000, v71
	v_lshlrev_b32_e32 v28, 16, v73
	v_and_b32_e32 v29, 0xffff0000, v73
	v_pk_mul_f32 v[70:71], v[80:81], v[80:81]
	v_mov_b32_e32 v73, v87
	v_mul_f32_e32 v72, v83, v83
	v_mul_f32_e32 v86, v85, v85
	v_pk_fma_f32 v[98:99], v[76:77], v[76:77], v[24:25] op_sel_hi:[1,1,0]
	v_pk_fma_f32 v[100:101], v[74:75], v[74:75], v[26:27] op_sel_hi:[1,1,0]
	v_pk_fma_f32 v[70:71], v[78:79], v[78:79], v[70:71]
	v_pk_fma_f32 v[102:103], v[82:83], v[82:83], v[72:73] op_sel_hi:[1,1,0]
	v_pk_fma_f32 v[104:105], v[84:85], v[84:85], v[86:87] op_sel_hi:[1,1,0]
	v_mov_b32_e32 v86, v100
	v_mov_b32_e32 v72, v98
	v_mul_f32_e32 v111, v89, v89
	v_mul_f32_e32 v112, v90, v90
	v_mul_f32_e32 v113, v91, v91
	v_pk_add_f32 v[98:99], v[100:101], v[98:99]
	v_pk_add_f32 v[70:71], v[70:71], v[70:71] op_sel:[0,1] op_sel_hi:[1,0]
	v_pk_mul_f32 v[72:73], v[86:87], v[72:73]
	v_and_b32_e32 v41, 0xffff0000, v35
	v_and_b32_e32 v40, 0xffff0000, v34
	v_mov_b32_e32 v103, v112
	v_mov_b32_e32 v105, v113
	v_mov_b32_e32 v71, v111
	v_mov_b32_e32 v99, v73
	v_lshlrev_b32_e32 v39, 16, v35
	v_lshlrev_b32_e32 v38, 16, v34
	v_pk_mul_f32 v[92:93], v[40:41], v[40:41]
	v_pk_add_f32 v[100:101], v[102:103], v[104:105]
	v_pk_add_f32 v[70:71], v[98:99], v[70:71]
	v_lshlrev_b32_e32 v35, 16, v37
	v_lshlrev_b32_e32 v34, 16, v36
	v_and_b32_e32 v37, 0xffff0000, v37
	v_and_b32_e32 v36, 0xffff0000, v36
	v_pk_fma_f32 v[92:93], v[38:39], v[38:39], v[92:93]
	v_pk_add_f32 v[70:71], v[70:71], v[100:101]
	v_pk_mul_f32 v[94:95], v[36:37], v[36:37]
	v_mov_b32_e32 v97, v27
	v_mul_f32_e32 v96, v33, v33
	v_pk_add_f32 v[92:93], v[92:93], v[92:93] op_sel:[0,1] op_sel_hi:[1,0]
	v_pk_add_f32 v[70:71], v[70:71], v[70:71] op_sel:[0,1] op_sel_hi:[1,0]
	v_mul_f32_e32 v88, v31, v31
	v_pk_fma_f32 v[94:95], v[34:35], v[34:35], v[94:95]
	v_pk_fma_f32 v[108:109], v[32:33], v[32:33], v[96:97] op_sel_hi:[1,1,0]
	v_mov_b32_e32 v96, v92
	v_mov_b32_e32 v26, v70
	v_mul_f32_e32 v114, v25, v25
	v_mul_f32_e32 v115, v28, v28
	v_mul_f32_e32 v116, v29, v29
	v_pk_fma_f32 v[106:107], v[30:31], v[30:31], v[88:89] op_sel_hi:[1,1,0]
	v_pk_add_f32 v[94:95], v[94:95], v[94:95] op_sel:[0,1] op_sel_hi:[1,0]
	v_pk_add_f32 v[70:71], v[70:71], v[92:93]
	v_pk_mul_f32 v[72:73], v[26:27], v[96:97]
	v_mov_b32_e32 v107, v115
	v_mov_b32_e32 v109, v116
	v_mov_b32_e32 v95, v114
	v_mov_b32_e32 v71, v73
	v_pk_add_f32 v[102:103], v[106:107], v[108:109]
	v_pk_add_f32 v[70:71], v[70:71], v[94:95]
	s_waitcnt vmcnt(0)
; #define GAS __attribute__((address_space(1)))
; __device__ __forceinline__ unsigned pk2(float lo, float hi) { return pg8::cvt_pk_bf16(lo, hi); }
; __device__ __forceinline__ unsigned pk4_fp8(float a, float b, float c, float d) { int p = 0; p = __builtin_amdgcn_cvt_pk_fp8_f32(a, b, p, false); p = __builtin_amdgcn_cvt_pk_fp8_f32(c, d, p, true); return (unsigned)p; }
; __device__ __forceinline__ float clamp8(float x) { return __builtin_fminf(__builtin_fmaxf(x, -448.0f), 448.0f); }
; template <bool F8, bool SRCH = false> __device__ __forceinline__ void norm_phase(Frame& F, const float* srcL, const float* srcC, const float* g, const float* mod, int shift_off, int scale_off, int nrows) {
;     ...
;         const float rstd = 1.0f / sqrtf(wave_sum(s) * (1.0f / DM) + NORM_EPS);
;         GAS v2u* o8 = (GAS v2u*)(XN + (size_t)row * DM) + F.lane;
; #pragma unroll
;         for (int j = 0; j < 8; ++j) { const int col = 4 * (F.lane + 64 * j);
;             const f32x4 gg = *(const GAS f32x4*)(g + col), sh = *(const GAS f32x4*)(mv + shift_off + col), sc = *(const GAS f32x4*)(mv + scale_off + col);
;             const f32x4 y = v[j] * rstd * gg * (sc + 1.0f) + sh;
;             if (F8) { ((GAS unsigned*)((unsigned char*)XN + (size_t)row * DM))[F.lane + 64 * j] = pk4_fp8(clamp8(y.x), clamp8(y.y), clamp8(y.z), clamp8(y.w)); }
;             else { v2u w; w.x = pk2(y.x, y.y); w.y = pk2(y.z, y.w); o8[64 * j] = w; } }
	v_pk_add_f32 v[66:67], v[66:67], 1.0 op_sel_hi:[1,0]
	v_pk_add_f32 v[70:71], v[70:71], v[102:103]
	v_pk_add_f32 v[68:69], v[68:69], 1.0 op_sel_hi:[1,0]
	v_add_f32_e32 v24, v70, v71
	ds_bpermute_b32 v26, v1, v24
	v_mov_b32_e32 v88, v87
	s_waitcnt lgkmcnt(0)
	v_add_f32_e32 v24, v24, v26
	ds_bpermute_b32 v26, v42, v24
	s_waitcnt lgkmcnt(0)
	v_add_f32_e32 v24, v24, v26
	ds_bpermute_b32 v26, v43, v24
	s_waitcnt lgkmcnt(0)
	v_add_f32_e32 v24, v24, v26
	ds_bpermute_b32 v26, v44, v24
	s_waitcnt lgkmcnt(0)
	v_add_f32_e32 v24, v24, v26
	ds_bpermute_b32 v26, v45, v24
	s_waitcnt lgkmcnt(0)
	v_add_f32_e32 v24, v24, v26
	ds_bpermute_b32 v26, v46, v24
	s_waitcnt lgkmcnt(0)
	v_add_f32_e32 v24, v24, v26
	v_fmamk_f32 v24, v24, 0x3a000000, v47
	v_mul_f32_e32 v26, 0x4f800000, v24
	v_cmp_gt_f32_e32 vcc, s5, v24
	s_nop 1
	v_cndmask_b32_e32 v24, v24, v26, vcc
	v_sqrt_f32_e32 v26, v24
	s_nop 0
	v_add_u32_e32 v70, -1, v26
	v_add_u32_e32 v71, 1, v26
	v_fma_f32 v72, -v70, v26, v24
	v_fma_f32 v73, -v71, v26, v24
	v_cmp_ge_f32_e64 s[0:1], 0, v72
	s_nop 1
	v_cndmask_b32_e64 v26, v26, v70, s[0:1]
	v_cmp_lt_f32_e64 s[0:1], 0, v73
	s_nop 1
	v_cndmask_b32_e64 v26, v26, v71, s[0:1]
	v_mul_f32_e32 v70, 0x37800000, v26
	v_cndmask_b32_e32 v26, v26, v70, vcc
	v_cmp_class_f32_e32 vcc, v24, v48
	s_nop 1
	v_cndmask_b32_e32 v24, v26, v24, vcc
	v_div_scale_f32 v26, s[0:1], v24, v24, 1.0
	v_rcp_f32_e32 v71, v26
	v_div_scale_f32 v70, vcc, 1.0, v24, 1.0
	v_fma_f32 v72, -v26, v71, 1.0
	v_fmac_f32_e32 v71, v72, v71
	v_mul_f32_e32 v72, v70, v71
	v_fma_f32 v73, -v26, v72, v70
	v_fmac_f32_e32 v72, v73, v71
	v_fma_f32 v26, -v26, v72, v70
	v_div_fmas_f32 v26, v26, v71, v72
	v_div_fixup_f32 v26, v26, v24, 1.0
	v_pk_mul_f32 v[72:73], v[26:27], v[74:75] op_sel_hi:[0,1]
	v_pk_mul_f32 v[58:59], v[58:59], v[72:73]
	v_pk_mul_f32 v[70:71], v[26:27], v[76:77] op_sel_hi:[0,1]
	v_pk_fma_f32 v[58:59], v[66:67], v[58:59], v[62:63]
	v_pk_mul_f32 v[60:61], v[60:61], v[70:71]
	v_med3_f32 v24, v58, s7, v57
	v_med3_f32 v58, v59, s7, v57
	v_cvt_pk_fp8_f32 v110, v24, v58
	v_pk_fma_f32 v[60:61], v[68:69], v[60:61], v[64:65]
	v_mov_b32_e32 v70, v79
	v_med3_f32 v59, v60, s7, v57
	v_med3_f32 v60, v61, s7, v57
	v_cvt_pk_fp8_f32 v110, v59, v60 op_sel:[0,0,1]
	v_mov_b32_e32 v79, v80
	v_pk_mul_f32 v[72:73], v[26:27], v[78:79] op_sel_hi:[0,1]
	v_mov_b32_e32 v24, 0
	global_store_dword v[22:23], v110, off
	v_mov_b32_e32 v58, v118
	v_mov_b32_e32 v59, v119
	v_mov_b32_e32 v60, v120
	v_mov_b32_e32 v61, v121
	v_mov_b32_e32 v62, v122
	v_mov_b32_e32 v63, v123
	v_mov_b32_e32 v64, v124
	v_mov_b32_e32 v65, v125
	v_mov_b32_e32 v66, v126
	v_mov_b32_e32 v67, v127
	v_mov_b32_e32 v68, v128
	v_mov_b32_e32 v69, v129
	v_mov_b32_e32 v71, v81
	v_pk_mul_f32 v[70:71], v[26:27], v[70:71] op_sel_hi:[0,1]
	v_pk_mul_f32 v[32:33], v[26:27], v[32:33] op_sel_hi:[0,1]
	v_pk_mul_f32 v[30:31], v[26:27], v[30:31] op_sel_hi:[0,1]
	v_pk_mul_f32 v[28:29], v[28:29], v[26:27] op_sel_hi:[1,0]
	v_pk_mul_f32 v[58:59], v[58:59], v[72:73]
	v_pk_add_f32 v[62:63], v[62:63], 1.0 op_sel_hi:[1,0]
	v_pk_mul_f32 v[60:61], v[60:61], v[70:71]
	v_pk_fma_f32 v[58:59], v[62:63], v[58:59], v[66:67]
	v_pk_add_f32 v[64:65], v[64:65], 1.0 op_sel_hi:[1,0]
	v_med3_f32 v58, v58, s7, v57
	v_med3_f32 v59, v59, s7, v57
	v_cvt_pk_fp8_f32 v24, v58, v59
	v_pk_fma_f32 v[60:61], v[64:65], v[60:61], v[68:69]
	v_pk_mul_f32 v[72:73], v[26:27], v[82:83] op_sel_hi:[0,1]
	v_med3_f32 v60, v60, s7, v57
	v_med3_f32 v61, v61, s7, v57
	v_cvt_pk_fp8_f32 v24, v60, v61 op_sel:[0,0,1]
	v_pk_mul_f32 v[70:71], v[26:27], v[84:85] op_sel_hi:[0,1]
	global_store_dword v[22:23], v24, off offset:256
	v_mov_b32_e32 v58, v130
	v_mov_b32_e32 v59, v131
	v_mov_b32_e32 v60, v132
	v_mov_b32_e32 v61, v133
	v_mov_b32_e32 v62, v134
	v_mov_b32_e32 v63, v135
	v_mov_b32_e32 v64, v136
	v_mov_b32_e32 v65, v137
	v_mov_b32_e32 v66, v138
	v_mov_b32_e32 v67, v139
	v_mov_b32_e32 v68, v140
	v_mov_b32_e32 v69, v141
	v_mov_b32_e32 v24, 0
	v_pk_mul_f32 v[58:59], v[58:59], v[72:73]
	v_pk_add_f32 v[62:63], v[62:63], 1.0 op_sel_hi:[1,0]
	v_pk_mul_f32 v[60:61], v[60:61], v[70:71]
	v_pk_fma_f32 v[58:59], v[58:59], v[62:63], v[66:67]
	v_pk_add_f32 v[64:65], v[64:65], 1.0 op_sel_hi:[1,0]
	v_med3_f32 v58, v58, s7, v57
	v_med3_f32 v59, v59, s7, v57
	v_cvt_pk_fp8_f32 v24, v58, v59
	v_pk_fma_f32 v[60:61], v[60:61], v[64:65], v[68:69]
	v_pk_mul_f32 v[72:73], v[88:89], v[26:27] op_sel_hi:[1,0]
	v_med3_f32 v60, v60, s7, v57
	v_med3_f32 v61, v61, s7, v57
	v_cvt_pk_fp8_f32 v24, v60, v61 op_sel:[0,0,1]
	v_pk_mul_f32 v[70:71], v[90:91], v[26:27] op_sel_hi:[1,0]
	global_store_dword v[22:23], v24, off offset:512
	v_mov_b32_e32 v58, v142
	v_mov_b32_e32 v59, v143
	v_mov_b32_e32 v60, v144
	v_mov_b32_e32 v61, v145
	v_mov_b32_e32 v62, v146
	v_mov_b32_e32 v63, v147
; #define GAS __attribute__((address_space(1)))
; __device__ __forceinline__ unsigned pk2(float lo, float hi) { return pg8::cvt_pk_bf16(lo, hi); }
; __device__ __forceinline__ unsigned pk4_fp8(float a, float b, float c, float d) { int p = 0; p = __builtin_amdgcn_cvt_pk_fp8_f32(a, b, p, false); p = __builtin_amdgcn_cvt_pk_fp8_f32(c, d, p, true); return (unsigned)p; }
; __device__ __forceinline__ float clamp8(float x) { return __builtin_fminf(__builtin_fmaxf(x, -448.0f), 448.0f); }
; template <bool F8, bool SRCH = false> __device__ __forceinline__ void norm_phase(Frame& F, const float* srcL, const float* srcC, const float* g, const float* mod, int shift_off, int scale_off, int nrows) {
;     ...
; #pragma unroll
;         for (int j = 0; j < 8; ++j) { const int col = 4 * (F.lane + 64 * j);
;             const f32x4 gg = *(const GAS f32x4*)(g + col), sh = *(const GAS f32x4*)(mv + shift_off + col), sc = *(const GAS f32x4*)(mv + scale_off + col);
;             const f32x4 y = v[j] * rstd * gg * (sc + 1.0f) + sh;
;             if (F8) { ((GAS unsigned*)((unsigned char*)XN + (size_t)row * DM))[F.lane + 64 * j] = pk4_fp8(clamp8(y.x), clamp8(y.y), clamp8(y.z), clamp8(y.w)); }
;             else { v2u w; w.x = pk2(y.x, y.y); w.y = pk2(y.z, y.w); o8[64 * j] = w; } }
	v_mov_b32_e32 v64, v148
	v_mov_b32_e32 v65, v149
	v_mov_b32_e32 v66, v150
	v_mov_b32_e32 v67, v151
	v_mov_b32_e32 v68, v152
	v_mov_b32_e32 v69, v153
	v_mov_b32_e32 v24, 0
	v_pk_mul_f32 v[58:59], v[72:73], v[58:59]
	v_pk_add_f32 v[62:63], v[62:63], 1.0 op_sel_hi:[1,0]
	v_pk_mul_f32 v[60:61], v[70:71], v[60:61]
	v_pk_fma_f32 v[58:59], v[58:59], v[62:63], v[66:67]
	v_pk_add_f32 v[64:65], v[64:65], 1.0 op_sel_hi:[1,0]
	v_med3_f32 v58, v58, s7, v57
	v_med3_f32 v59, v59, s7, v57
	v_cvt_pk_fp8_f32 v24, v58, v59
	v_pk_fma_f32 v[60:61], v[60:61], v[64:65], v[68:69]
	v_mov_b32_e32 v70, v39
	v_med3_f32 v60, v60, s7, v57
	v_med3_f32 v61, v61, s7, v57
	v_cvt_pk_fp8_f32 v24, v60, v61 op_sel:[0,0,1]
	v_mov_b32_e32 v71, v41
	v_mov_b32_e32 v39, v40
	v_pk_mul_f32 v[40:41], v[26:27], v[70:71] op_sel_hi:[0,1]
	global_store_dword v[22:23], v24, off offset:768
	v_mov_b32_e32 v58, v154
	v_mov_b32_e32 v59, v155
	v_mov_b32_e32 v60, v156
	v_mov_b32_e32 v61, v157
	v_mov_b32_e32 v62, v158
	v_mov_b32_e32 v63, v159
	v_mov_b32_e32 v64, v160
	v_mov_b32_e32 v65, v161
	v_mov_b32_e32 v66, v162
	v_mov_b32_e32 v67, v163
	v_mov_b32_e32 v68, v164
	v_mov_b32_e32 v69, v165
	v_pk_mul_f32 v[38:39], v[26:27], v[38:39] op_sel_hi:[0,1]
	v_mov_b32_e32 v24, 0
	v_pk_mul_f32 v[38:39], v[38:39], v[58:59]
	v_pk_mul_f32 v[40:41], v[40:41], v[60:61]
	v_pk_add_f32 v[60:61], v[62:63], 1.0 op_sel_hi:[1,0]
	v_pk_add_f32 v[58:59], v[64:65], 1.0 op_sel_hi:[1,0]
	v_pk_fma_f32 v[38:39], v[38:39], v[60:61], v[66:67]
	v_pk_fma_f32 v[40:41], v[40:41], v[58:59], v[68:69]
	v_med3_f32 v38, v38, s7, v57
	v_med3_f32 v39, v39, s7, v57
	v_cvt_pk_fp8_f32 v24, v38, v39
	v_med3_f32 v40, v40, s7, v57
	v_med3_f32 v41, v41, s7, v57
	v_mov_b32_e32 v66, v35
	v_cvt_pk_fp8_f32 v24, v40, v41 op_sel:[0,0,1]
	v_mov_b32_e32 v67, v37
	v_mov_b32_e32 v35, v36
	v_pk_mul_f32 v[36:37], v[26:27], v[66:67] op_sel_hi:[0,1]
	global_store_dword v[22:23], v24, off offset:1024
	v_mov_b32_e32 v38, v166
	v_mov_b32_e32 v39, v167
	v_mov_b32_e32 v40, v168
	v_mov_b32_e32 v41, v169
	v_mov_b32_e32 v58, v170
	v_mov_b32_e32 v59, v171
	v_mov_b32_e32 v60, v172
	v_mov_b32_e32 v61, v173
	v_mov_b32_e32 v62, v174
	v_mov_b32_e32 v63, v175
	v_mov_b32_e32 v64, v176
	v_mov_b32_e32 v65, v177
	v_pk_mul_f32 v[34:35], v[26:27], v[34:35] op_sel_hi:[0,1]
	v_mov_b32_e32 v24, 0
	v_pk_mul_f32 v[34:35], v[34:35], v[38:39]
	v_pk_mul_f32 v[36:37], v[36:37], v[40:41]
	v_pk_add_f32 v[40:41], v[58:59], 1.0 op_sel_hi:[1,0]
	v_pk_add_f32 v[38:39], v[60:61], 1.0 op_sel_hi:[1,0]
	v_pk_fma_f32 v[34:35], v[34:35], v[40:41], v[62:63]
	v_pk_fma_f32 v[36:37], v[36:37], v[38:39], v[64:65]
	v_med3_f32 v34, v34, s7, v57
	v_med3_f32 v35, v35, s7, v57
	v_cvt_pk_fp8_f32 v24, v34, v35
	v_med3_f32 v36, v36, s7, v57
	v_med3_f32 v37, v37, s7, v57
	v_cvt_pk_fp8_f32 v24, v36, v37 op_sel:[0,0,1]
	global_store_dword v[22:23], v24, off offset:1280
	v_mov_b32_e32 v34, v182
	v_mov_b32_e32 v35, v183
	v_mov_b32_e32 v36, v184
	v_mov_b32_e32 v37, v185
	v_mov_b32_e32 v38, v186
	v_mov_b32_e32 v39, v187
	v_mov_b32_e32 v40, v188
	v_mov_b32_e32 v41, v189
	v_mov_b32_e32 v58, v190
	v_mov_b32_e32 v59, v191
	v_mov_b32_e32 v60, v192
	v_mov_b32_e32 v61, v193
	v_mov_b32_e32 v24, 0
	v_pk_mul_f32 v[30:31], v[30:31], v[34:35]
	v_pk_mul_f32 v[32:33], v[32:33], v[36:37]
	v_pk_add_f32 v[36:37], v[38:39], 1.0 op_sel_hi:[1,0]
	v_pk_add_f32 v[34:35], v[40:41], 1.0 op_sel_hi:[1,0]
	v_pk_fma_f32 v[30:31], v[30:31], v[36:37], v[58:59]
	v_pk_fma_f32 v[32:33], v[32:33], v[34:35], v[60:61]
	v_med3_f32 v30, v30, s7, v57
	v_med3_f32 v31, v31, s7, v57
	v_cvt_pk_fp8_f32 v24, v30, v31
	v_med3_f32 v32, v32, s7, v57
	v_med3_f32 v33, v33, s7, v57
	v_mov_b32_e32 v58, 0
	v_cvt_pk_fp8_f32 v24, v32, v33 op_sel:[0,0,1]
	global_store_dword v[22:23], v24, off offset:1536
	v_mov_b32_e32 v30, v194
	v_mov_b32_e32 v31, v195
	v_mov_b32_e32 v32, v196
	v_mov_b32_e32 v33, v197
	v_mov_b32_e32 v34, v198
	v_mov_b32_e32 v35, v199
	v_mov_b32_e32 v36, v200
	v_mov_b32_e32 v37, v201
	v_mov_b32_e32 v38, v202
	v_mov_b32_e32 v39, v203
	v_mov_b32_e32 v40, v204
	v_mov_b32_e32 v41, v205
	v_mov_b32_e32 v24, v27
	v_pk_mul_f32 v[24:25], v[24:25], v[26:27] op_sel_hi:[1,0]
	v_pk_mul_f32 v[26:27], v[28:29], v[32:33]
	v_pk_mul_f32 v[24:25], v[24:25], v[30:31]
	v_pk_add_f32 v[30:31], v[34:35], 1.0 op_sel_hi:[1,0]
	v_pk_add_f32 v[28:29], v[36:37], 1.0 op_sel_hi:[1,0]
	v_pk_fma_f32 v[24:25], v[24:25], v[30:31], v[38:39]
	s_nop 0
	v_med3_f32 v24, v24, s7, v57
	v_med3_f32 v25, v25, s7, v57
	v_cvt_pk_fp8_f32 v58, v24, v25
	v_pk_fma_f32 v[24:25], v[26:27], v[28:29], v[40:41]
	s_nop 0
	v_med3_f32 v24, v24, s7, v57
	v_med3_f32 v25, v25, s7, v57
	v_cvt_pk_fp8_f32 v58, v24, v25 op_sel:[0,0,1]
	global_store_dword v[22:23], v58, off offset:1792
	s_cbranch_scc1 .LBB0_603

; #define GAS __attribute__((address_space(1)))
; template <bool F8, bool SRCH = false> __device__ __forceinline__ void norm_phase(Frame& F, const float* srcL, const float* srcC, const float* g, const float* mod, int shift_off, int scale_off, int nrows) {
;     ...
;     for (int row = gw; row < nrows; row += NGW) {
;         const float* src = row < ML ? srcL + (size_t)row * DM : srcC + (size_t)(row - ML) * DM;
;         const float* mv = mod + (size_t)(row < ML ? (row >> 13) : 2) * MOD_W;
;         const GAS f32x4* xr = (const GAS f32x4*)src + F.lane;
;         f32x4 v[8]; float s = 0.f;
; #pragma unroll
;         for (int j = 0; j < 8; ++j) {
;             if constexpr (SRCH) { const v2u w = ((const GAS v2u*)(WSP(const bf16, WS_H) + (size_t)row * DM))[F.lane + 64 * j]; v[j].x = bflo(w.x); v[j].y = bfhi(w.x); v[j].z = bflo(w.y); v[j].w = bfhi(w.y); }
;             else v[j] = xr[64 * j];
;             s += (v[j].x * v[j].x + v[j].y * v[j].y) + (v[j].z * v[j].z + v[j].w * v[j].w); }
;         const float rstd = 1.0f / sqrtf(wave_sum(s) * (1.0f / DM) + NORM_EPS);
.LBB0_1067:
	global_load_dwordx2 v[14:15], v[12:13], off
	global_load_dwordx2 v[16:17], v[12:13], off offset:512
	global_load_dwordx2 v[18:19], v[12:13], off offset:1024
	global_load_dwordx2 v[20:21], v[12:13], off offset:1536
	global_load_dwordx2 v[22:23], v[12:13], off offset:2048
	global_load_dwordx2 v[26:27], v[12:13], off offset:2560
	global_load_dwordx2 v[56:57], v[12:13], off offset:3072
	global_load_dwordx2 v[58:59], v[12:13], off offset:3584
	s_min_i32 s0, s4, 0x4000
	s_ashr_i32 s0, s0, 13
	s_mul_hi_i32 s1, s0, 0xc000
	s_mul_i32 s0, s0, 0xc000
	s_add_u32 s10, s14, s0
	s_addc_u32 s11, s15, s1
	s_add_u32 s12, s10, 0x2000
	s_addc_u32 s13, s11, 0
	global_load_dwordx4 v[44:47], v[2:3], off
	global_load_dwordx4 v[48:51], v35, s[10:11]
	global_load_dwordx4 v[52:55], v35, s[12:13]
	global_load_dwordx4 v[108:111], v[2:3], off offset:1024
	global_load_dwordx4 v[112:115], v36, s[12:13]
	global_load_dwordx4 v[116:119], v35, s[10:11] offset:1024
	global_load_dwordx4 v[120:123], v[2:3], off offset:2048
	global_load_dwordx4 v[124:127], v37, s[12:13]
	global_load_dwordx4 v[128:131], v35, s[10:11] offset:2048
	global_load_dwordx4 v[132:135], v[2:3], off offset:3072
	global_load_dwordx4 v[136:139], v38, s[12:13]
	global_load_dwordx4 v[140:143], v35, s[10:11] offset:3072
	global_load_dwordx4 v[144:147], v[4:5], off
	global_load_dwordx4 v[148:151], v39, s[12:13]
	global_load_dwordx4 v[152:155], v39, s[10:11]
	global_load_dwordx4 v[156:159], v[6:7], off
	global_load_dwordx4 v[160:163], v40, s[12:13]
	global_load_dwordx4 v[164:167], v40, s[10:11]
	global_load_dwordx4 v[168:171], v[8:9], off
	global_load_dwordx4 v[172:175], v41, s[12:13]
	global_load_dwordx4 v[182:185], v41, s[10:11]
	global_load_dwordx4 v[186:189], v[10:11], off
	global_load_dwordx4 v[190:193], v42, s[12:13]
	global_load_dwordx4 v[194:197], v42, s[10:11]
	v_add_co_u32_e32 v60, vcc, s7, v12
	s_add_i32 s4, s4, s6
	s_nop 0
	v_addc_co_u32_e32 v61, vcc, -1, v13, vcc
	s_cmpk_lt_i32 s4, 0x4200
	s_waitcnt vmcnt(31)
	v_and_b32_e32 v63, 0xffff0000, v14
	v_and_b32_e32 v65, 0xffff0000, v15
	v_lshlrev_b32_e32 v62, 16, v14
	v_lshlrev_b32_e32 v64, 16, v15
	s_waitcnt vmcnt(30)
	v_lshlrev_b32_e32 v67, 16, v17
	v_lshlrev_b32_e32 v66, 16, v16
	v_and_b32_e32 v69, 0xffff0000, v17
	v_and_b32_e32 v68, 0xffff0000, v16
	s_waitcnt vmcnt(29)
	v_and_b32_e32 v71, 0xffff0000, v18
	v_and_b32_e32 v73, 0xffff0000, v19
	s_waitcnt vmcnt(28)
	v_lshlrev_b32_e32 v75, 16, v20
	s_waitcnt vmcnt(24)
	v_lshlrev_b32_e32 v17, 16, v58
	v_and_b32_e32 v15, 0xffff0000, v58
	v_mul_f32_e32 v14, v65, v65
	v_mul_f32_e32 v16, v63, v63
	v_lshlrev_b32_e32 v70, 16, v18
	v_lshlrev_b32_e32 v72, 16, v19
	v_and_b32_e32 v77, 0xffff0000, v20
	v_lshlrev_b32_e32 v78, 16, v21
	v_and_b32_e32 v79, 0xffff0000, v21
	v_lshlrev_b32_e32 v81, 16, v23
	v_lshlrev_b32_e32 v80, 16, v22
	v_and_b32_e32 v83, 0xffff0000, v23
	v_and_b32_e32 v82, 0xffff0000, v22
	v_lshlrev_b32_e32 v20, 16, v56
	v_and_b32_e32 v21, 0xffff0000, v56
	v_lshlrev_b32_e32 v22, 16, v57
	v_and_b32_e32 v23, 0xffff0000, v57
	v_lshlrev_b32_e32 v18, 16, v59
	v_and_b32_e32 v19, 0xffff0000, v59
	v_pk_mul_f32 v[56:57], v[68:69], v[68:69]
	v_mov_b32_e32 v59, v75
	v_mul_f32_e32 v58, v71, v71
	v_mul_f32_e32 v74, v73, v73
	v_pk_fma_f32 v[90:91], v[64:65], v[64:65], v[14:15] op_sel_hi:[1,1,0]
	v_pk_fma_f32 v[92:93], v[62:63], v[62:63], v[16:17] op_sel_hi:[1,1,0]
	v_pk_fma_f32 v[56:57], v[66:67], v[66:67], v[56:57]
	v_pk_fma_f32 v[94:95], v[70:71], v[70:71], v[58:59] op_sel_hi:[1,1,0]
	v_pk_fma_f32 v[96:97], v[72:73], v[72:73], v[74:75] op_sel_hi:[1,1,0]
	v_mov_b32_e32 v74, v92
	v_mov_b32_e32 v58, v90
	v_mul_f32_e32 v43, v77, v77
	v_mul_f32_e32 v102, v78, v78
	v_mul_f32_e32 v103, v79, v79
	v_pk_add_f32 v[90:91], v[92:93], v[90:91]
	v_pk_add_f32 v[56:57], v[56:57], v[56:57] op_sel:[0,1] op_sel_hi:[1,0]
	v_pk_mul_f32 v[58:59], v[74:75], v[58:59]
	v_mov_b32_e32 v95, v102
	v_mov_b32_e32 v97, v103
	v_mov_b32_e32 v57, v43
	v_mov_b32_e32 v91, v59
	v_pk_mul_f32 v[84:85], v[82:83], v[82:83]
	v_pk_add_f32 v[92:93], v[94:95], v[96:97]
	v_pk_add_f32 v[56:57], v[90:91], v[56:57]
	v_lshlrev_b32_e32 v25, 16, v27
	v_lshlrev_b32_e32 v24, 16, v26
	v_and_b32_e32 v27, 0xffff0000, v27
	v_and_b32_e32 v26, 0xffff0000, v26
	v_pk_fma_f32 v[84:85], v[80:81], v[80:81], v[84:85]
	v_pk_add_f32 v[56:57], v[56:57], v[92:93]
	v_pk_mul_f32 v[86:87], v[26:27], v[26:27]
	v_mov_b32_e32 v89, v17
	v_mul_f32_e32 v88, v23, v23
	v_pk_add_f32 v[84:85], v[84:85], v[84:85] op_sel:[0,1] op_sel_hi:[1,0]
	v_pk_add_f32 v[56:57], v[56:57], v[56:57] op_sel:[0,1] op_sel_hi:[1,0]
	v_mul_f32_e32 v76, v21, v21
	v_pk_fma_f32 v[86:87], v[24:25], v[24:25], v[86:87]
	v_pk_fma_f32 v[100:101], v[22:23], v[22:23], v[88:89] op_sel_hi:[1,1,0]
	v_mov_b32_e32 v88, v84
	v_mov_b32_e32 v16, v56
	v_mul_f32_e32 v104, v15, v15
	v_mul_f32_e32 v105, v18, v18
	v_mul_f32_e32 v106, v19, v19
	v_pk_fma_f32 v[98:99], v[20:21], v[20:21], v[76:77] op_sel_hi:[1,1,0]
	v_pk_add_f32 v[86:87], v[86:87], v[86:87] op_sel:[0,1] op_sel_hi:[1,0]
	v_pk_add_f32 v[56:57], v[56:57], v[84:85]
	v_pk_mul_f32 v[58:59], v[16:17], v[88:89]
	v_mov_b32_e32 v99, v105
	v_mov_b32_e32 v101, v106
	v_mov_b32_e32 v87, v104
	v_mov_b32_e32 v57, v59
	v_pk_add_f32 v[94:95], v[98:99], v[100:101]
	v_pk_add_f32 v[56:57], v[56:57], v[86:87]
	s_waitcnt vmcnt(0)
	v_pk_add_f32 v[52:53], v[52:53], 1.0 op_sel_hi:[1,0]
	v_pk_add_f32 v[56:57], v[56:57], v[94:95]
	v_pk_add_f32 v[54:55], v[54:55], 1.0 op_sel_hi:[1,0]
	v_add_f32_e32 v14, v56, v57
	ds_bpermute_b32 v16, v1, v14
	v_mov_b32_e32 v76, v75
	s_waitcnt lgkmcnt(0)
	v_add_f32_e32 v14, v14, v16
	ds_bpermute_b32 v16, v28, v14
	s_waitcnt lgkmcnt(0)
; #define GAS __attribute__((address_space(1)))
; __device__ __forceinline__ unsigned pk2(float lo, float hi) { return pg8::cvt_pk_bf16(lo, hi); }
; __device__ __forceinline__ unsigned pk4_fp8(float a, float b, float c, float d) { int p = 0; p = __builtin_amdgcn_cvt_pk_fp8_f32(a, b, p, false); p = __builtin_amdgcn_cvt_pk_fp8_f32(c, d, p, true); return (unsigned)p; }
; __device__ __forceinline__ float clamp8(float x) { return __builtin_fminf(__builtin_fmaxf(x, -448.0f), 448.0f); }
; template <bool F8, bool SRCH = false> __device__ __forceinline__ void norm_phase(Frame& F, const float* srcL, const float* srcC, const float* g, const float* mod, int shift_off, int scale_off, int nrows) {
;     ...
;         const float rstd = 1.0f / sqrtf(wave_sum(s) * (1.0f / DM) + NORM_EPS);
;         GAS v2u* o8 = (GAS v2u*)(XN + (size_t)row * DM) + F.lane;
; #pragma unroll
;         for (int j = 0; j < 8; ++j) { const int col = 4 * (F.lane + 64 * j);
;             const f32x4 gg = *(const GAS f32x4*)(g + col), sh = *(const GAS f32x4*)(mv + shift_off + col), sc = *(const GAS f32x4*)(mv + scale_off + col);
;             const f32x4 y = v[j] * rstd * gg * (sc + 1.0f) + sh;
;             if (F8) { ((GAS unsigned*)((unsigned char*)XN + (size_t)row * DM))[F.lane + 64 * j] = pk4_fp8(clamp8(y.x), clamp8(y.y), clamp8(y.z), clamp8(y.w)); }
;             else { v2u w; w.x = pk2(y.x, y.y); w.y = pk2(y.z, y.w); o8[64 * j] = w; } }
	v_add_f32_e32 v14, v14, v16
	ds_bpermute_b32 v16, v29, v14
	s_waitcnt lgkmcnt(0)
	v_add_f32_e32 v14, v14, v16
	ds_bpermute_b32 v16, v30, v14
	s_waitcnt lgkmcnt(0)
	v_add_f32_e32 v14, v14, v16
	ds_bpermute_b32 v16, v31, v14
	s_waitcnt lgkmcnt(0)
	v_add_f32_e32 v14, v14, v16
	ds_bpermute_b32 v16, v32, v14
	s_waitcnt lgkmcnt(0)
	v_add_f32_e32 v14, v14, v16
	v_fmamk_f32 v14, v14, 0x3a000000, v33
	v_mul_f32_e32 v16, 0x4f800000, v14
	v_cmp_gt_f32_e32 vcc, s5, v14
	s_nop 1
	v_cndmask_b32_e32 v14, v14, v16, vcc
	v_sqrt_f32_e32 v16, v14
	s_nop 0
	v_add_u32_e32 v43, -1, v16
	v_add_u32_e32 v56, 1, v16
	v_fma_f32 v57, -v43, v16, v14
	v_fma_f32 v58, -v56, v16, v14
	v_cmp_ge_f32_e64 s[0:1], 0, v57
	s_nop 1
	v_cndmask_b32_e64 v16, v16, v43, s[0:1]
	v_cmp_lt_f32_e64 s[0:1], 0, v58
	s_nop 1
	v_cndmask_b32_e64 v16, v16, v56, s[0:1]
	v_mul_f32_e32 v43, 0x37800000, v16
	v_cndmask_b32_e32 v16, v16, v43, vcc
	v_cmp_class_f32_e32 vcc, v14, v34
	s_nop 1
	v_cndmask_b32_e32 v14, v16, v14, vcc
	v_div_scale_f32 v16, s[0:1], v14, v14, 1.0
	v_rcp_f32_e32 v56, v16
	v_div_scale_f32 v43, vcc, 1.0, v14, 1.0
	v_fma_f32 v57, -v16, v56, 1.0
	v_fmac_f32_e32 v56, v57, v56
	v_mul_f32_e32 v57, v43, v56
	v_fma_f32 v58, -v16, v57, v43
	v_fmac_f32_e32 v57, v58, v56
	v_fma_f32 v16, -v16, v57, v43
	v_div_fmas_f32 v16, v16, v56, v57
	v_div_fixup_f32 v16, v16, v14, 1.0
	v_pk_mul_f32 v[58:59], v[16:17], v[62:63] op_sel_hi:[0,1]
	v_pk_mul_f32 v[56:57], v[16:17], v[64:65] op_sel_hi:[0,1]
	v_pk_mul_f32 v[44:45], v[44:45], v[58:59]
	v_pk_mul_f32 v[46:47], v[46:47], v[56:57]
	v_pk_fma_f32 v[44:45], v[52:53], v[44:45], v[48:49]
	v_pk_fma_f32 v[46:47], v[54:55], v[46:47], v[50:51]
	v_cvt_pk_bf16_f32 v44, v44, v45
	v_mov_b32_e32 v58, v67
	v_cvt_pk_bf16_f32 v45, v46, v47
	global_store_dwordx2 v[60:61], v[44:45], off
	v_mov_b32_e32 v44, v108
	v_mov_b32_e32 v45, v109
	v_mov_b32_e32 v46, v110
	v_mov_b32_e32 v47, v111
	s_nop 0
	v_mov_b32_e32 v48, v112
	v_mov_b32_e32 v49, v113
	v_mov_b32_e32 v50, v114
	v_mov_b32_e32 v51, v115
	v_mov_b32_e32 v52, v116
	v_mov_b32_e32 v53, v117
	v_mov_b32_e32 v54, v118
	v_mov_b32_e32 v55, v119
	v_mov_b32_e32 v67, v68
	v_mov_b32_e32 v59, v69
	v_pk_mul_f32 v[60:61], v[16:17], v[66:67] op_sel_hi:[0,1]
	v_add_co_u32_e32 v56, vcc, s16, v12
	v_pk_mul_f32 v[58:59], v[16:17], v[58:59] op_sel_hi:[0,1]
	s_nop 0
	v_addc_co_u32_e32 v57, vcc, -1, v13, vcc
	v_pk_mul_f32 v[22:23], v[16:17], v[22:23] op_sel_hi:[0,1]
	v_pk_mul_f32 v[20:21], v[16:17], v[20:21] op_sel_hi:[0,1]
	v_mov_b32_e32 v14, v17
	v_pk_mul_f32 v[14:15], v[14:15], v[16:17] op_sel_hi:[1,0]
	v_pk_mul_f32 v[18:19], v[18:19], v[16:17] op_sel_hi:[1,0]
	v_lshl_add_u64 v[12:13], v[12:13], 0, s[8:9]
	v_pk_mul_f32 v[44:45], v[44:45], v[60:61]
	v_pk_add_f32 v[48:49], v[48:49], 1.0 op_sel_hi:[1,0]
	v_pk_mul_f32 v[46:47], v[46:47], v[58:59]
	v_pk_add_f32 v[50:51], v[50:51], 1.0 op_sel_hi:[1,0]
	v_pk_fma_f32 v[44:45], v[48:49], v[44:45], v[52:53]
	v_pk_fma_f32 v[46:47], v[50:51], v[46:47], v[54:55]
	v_cvt_pk_bf16_f32 v44, v44, v45
	v_pk_mul_f32 v[60:61], v[16:17], v[70:71] op_sel_hi:[0,1]
	v_cvt_pk_bf16_f32 v45, v46, v47
	global_store_dwordx2 v[56:57], v[44:45], off offset:-3584
	v_mov_b32_e32 v44, v120
	v_mov_b32_e32 v45, v121
	v_mov_b32_e32 v46, v122
	v_mov_b32_e32 v47, v123
	s_nop 0
	v_mov_b32_e32 v48, v124
	v_mov_b32_e32 v49, v125
	v_mov_b32_e32 v50, v126
	v_mov_b32_e32 v51, v127
	v_mov_b32_e32 v52, v128
	v_mov_b32_e32 v53, v129
	v_mov_b32_e32 v54, v130
	v_mov_b32_e32 v55, v131
	v_pk_mul_f32 v[58:59], v[16:17], v[72:73] op_sel_hi:[0,1]
	v_pk_mul_f32 v[44:45], v[44:45], v[60:61]
	v_pk_add_f32 v[48:49], v[48:49], 1.0 op_sel_hi:[1,0]
	v_pk_mul_f32 v[46:47], v[46:47], v[58:59]
	v_pk_add_f32 v[50:51], v[50:51], 1.0 op_sel_hi:[1,0]
	v_pk_fma_f32 v[44:45], v[44:45], v[48:49], v[52:53]
	v_pk_fma_f32 v[46:47], v[46:47], v[50:51], v[54:55]
	v_cvt_pk_bf16_f32 v44, v44, v45
	v_pk_mul_f32 v[60:61], v[76:77], v[16:17] op_sel_hi:[1,0]
	v_cvt_pk_bf16_f32 v45, v46, v47
	global_store_dwordx2 v[56:57], v[44:45], off offset:-3072
	v_mov_b32_e32 v44, v132
	v_mov_b32_e32 v45, v133
	v_mov_b32_e32 v46, v134
; #define GAS __attribute__((address_space(1)))
; __device__ __forceinline__ unsigned pk2(float lo, float hi) { return pg8::cvt_pk_bf16(lo, hi); }
; __device__ __forceinline__ unsigned pk4_fp8(float a, float b, float c, float d) { int p = 0; p = __builtin_amdgcn_cvt_pk_fp8_f32(a, b, p, false); p = __builtin_amdgcn_cvt_pk_fp8_f32(c, d, p, true); return (unsigned)p; }
; __device__ __forceinline__ float clamp8(float x) { return __builtin_fminf(__builtin_fmaxf(x, -448.0f), 448.0f); }
; template <bool F8, bool SRCH = false> __device__ __forceinline__ void norm_phase(Frame& F, const float* srcL, const float* srcC, const float* g, const float* mod, int shift_off, int scale_off, int nrows) {
;     ...
; #pragma unroll
;         for (int j = 0; j < 8; ++j) { const int col = 4 * (F.lane + 64 * j);
;             const f32x4 gg = *(const GAS f32x4*)(g + col), sh = *(const GAS f32x4*)(mv + shift_off + col), sc = *(const GAS f32x4*)(mv + scale_off + col);
;             const f32x4 y = v[j] * rstd * gg * (sc + 1.0f) + sh;
;             if (F8) { ((GAS unsigned*)((unsigned char*)XN + (size_t)row * DM))[F.lane + 64 * j] = pk4_fp8(clamp8(y.x), clamp8(y.y), clamp8(y.z), clamp8(y.w)); }
;             else { v2u w; w.x = pk2(y.x, y.y); w.y = pk2(y.z, y.w); o8[64 * j] = w; } }
	v_mov_b32_e32 v47, v135
	s_nop 0
	v_mov_b32_e32 v48, v136
	v_mov_b32_e32 v49, v137
	v_mov_b32_e32 v50, v138
	v_mov_b32_e32 v51, v139
	v_mov_b32_e32 v52, v140
	v_mov_b32_e32 v53, v141
	v_mov_b32_e32 v54, v142
	v_mov_b32_e32 v55, v143
	v_pk_mul_f32 v[58:59], v[78:79], v[16:17] op_sel_hi:[1,0]
	v_pk_mul_f32 v[44:45], v[60:61], v[44:45]
	v_pk_add_f32 v[48:49], v[48:49], 1.0 op_sel_hi:[1,0]
	v_pk_mul_f32 v[46:47], v[58:59], v[46:47]
	v_pk_add_f32 v[50:51], v[50:51], 1.0 op_sel_hi:[1,0]
	v_pk_fma_f32 v[44:45], v[44:45], v[48:49], v[52:53]
	v_pk_fma_f32 v[46:47], v[46:47], v[50:51], v[54:55]
	v_cvt_pk_bf16_f32 v44, v44, v45
	v_mov_b32_e32 v58, v81
	v_cvt_pk_bf16_f32 v45, v46, v47
	global_store_dwordx2 v[56:57], v[44:45], off offset:-2560
	v_mov_b32_e32 v44, v144
	v_mov_b32_e32 v45, v145
	v_mov_b32_e32 v46, v146
	v_mov_b32_e32 v47, v147
	s_nop 0
	v_mov_b32_e32 v48, v148
	v_mov_b32_e32 v49, v149
	v_mov_b32_e32 v50, v150
	v_mov_b32_e32 v51, v151
	v_mov_b32_e32 v52, v152
	v_mov_b32_e32 v53, v153
	v_mov_b32_e32 v54, v154
	v_mov_b32_e32 v55, v155
	v_mov_b32_e32 v81, v82
	v_mov_b32_e32 v59, v83
	v_pk_mul_f32 v[60:61], v[16:17], v[80:81] op_sel_hi:[0,1]
	v_pk_mul_f32 v[58:59], v[16:17], v[58:59] op_sel_hi:[0,1]
	v_pk_mul_f32 v[44:45], v[60:61], v[44:45]
	v_pk_add_f32 v[48:49], v[48:49], 1.0 op_sel_hi:[1,0]
	v_pk_mul_f32 v[46:47], v[58:59], v[46:47]
	v_pk_add_f32 v[50:51], v[50:51], 1.0 op_sel_hi:[1,0]
	v_pk_fma_f32 v[44:45], v[44:45], v[48:49], v[52:53]
	v_pk_fma_f32 v[46:47], v[46:47], v[50:51], v[54:55]
	v_cvt_pk_bf16_f32 v44, v44, v45
	v_mov_b32_e32 v58, v25
	v_cvt_pk_bf16_f32 v45, v46, v47
	global_store_dwordx2 v[56:57], v[44:45], off offset:-2048
	v_mov_b32_e32 v44, v156
	v_mov_b32_e32 v45, v157
	v_mov_b32_e32 v46, v158
	v_mov_b32_e32 v47, v159
	s_nop 0
	v_mov_b32_e32 v48, v160
	v_mov_b32_e32 v49, v161
	v_mov_b32_e32 v50, v162
	v_mov_b32_e32 v51, v163
	v_mov_b32_e32 v52, v164
	v_mov_b32_e32 v53, v165
	v_mov_b32_e32 v54, v166
	v_mov_b32_e32 v55, v167
	v_mov_b32_e32 v59, v27
	v_mov_b32_e32 v25, v26
	v_pk_mul_f32 v[26:27], v[16:17], v[58:59] op_sel_hi:[0,1]
	v_pk_mul_f32 v[24:25], v[16:17], v[24:25] op_sel_hi:[0,1]
	v_pk_mul_f32 v[24:25], v[24:25], v[44:45]
	v_pk_mul_f32 v[26:27], v[26:27], v[46:47]
	v_pk_add_f32 v[46:47], v[48:49], 1.0 op_sel_hi:[1,0]
	v_pk_add_f32 v[44:45], v[50:51], 1.0 op_sel_hi:[1,0]
	v_pk_fma_f32 v[24:25], v[24:25], v[46:47], v[52:53]
	v_pk_fma_f32 v[26:27], v[26:27], v[44:45], v[54:55]
	v_cvt_pk_bf16_f32 v24, v24, v25
	s_nop 0
	v_cvt_pk_bf16_f32 v25, v26, v27
	global_store_dwordx2 v[56:57], v[24:25], off offset:-1536
	v_mov_b32_e32 v24, v168
	v_mov_b32_e32 v25, v169
	v_mov_b32_e32 v26, v170
	v_mov_b32_e32 v27, v171
	s_nop 0
	v_mov_b32_e32 v44, v172
	v_mov_b32_e32 v45, v173
	v_mov_b32_e32 v46, v174
	v_mov_b32_e32 v47, v175
	v_mov_b32_e32 v48, v182
	v_mov_b32_e32 v49, v183
	v_mov_b32_e32 v50, v184
	v_mov_b32_e32 v51, v185
	v_pk_mul_f32 v[20:21], v[20:21], v[24:25]
	v_pk_mul_f32 v[22:23], v[22:23], v[26:27]
	v_pk_add_f32 v[26:27], v[44:45], 1.0 op_sel_hi:[1,0]
	v_pk_add_f32 v[24:25], v[46:47], 1.0 op_sel_hi:[1,0]
	v_pk_fma_f32 v[20:21], v[20:21], v[26:27], v[48:49]
	v_pk_fma_f32 v[22:23], v[22:23], v[24:25], v[50:51]
	v_cvt_pk_bf16_f32 v20, v20, v21
	s_nop 0
	v_cvt_pk_bf16_f32 v21, v22, v23
	global_store_dwordx2 v[56:57], v[20:21], off offset:-1024
	v_mov_b32_e32 v20, v186
	v_mov_b32_e32 v21, v187
	v_mov_b32_e32 v22, v188
	v_mov_b32_e32 v23, v189
	s_nop 0
	v_mov_b32_e32 v24, v190
	v_mov_b32_e32 v25, v191
	v_mov_b32_e32 v26, v192
	v_mov_b32_e32 v27, v193
	v_mov_b32_e32 v44, v194
	v_mov_b32_e32 v45, v195
	v_mov_b32_e32 v46, v196
	v_mov_b32_e32 v47, v197
	v_pk_mul_f32 v[14:15], v[14:15], v[20:21]
	v_pk_add_f32 v[20:21], v[24:25], 1.0 op_sel_hi:[1,0]
	v_pk_mul_f32 v[16:17], v[18:19], v[22:23]
	v_pk_add_f32 v[18:19], v[26:27], 1.0 op_sel_hi:[1,0]
	v_pk_fma_f32 v[14:15], v[14:15], v[20:21], v[44:45]
	v_pk_fma_f32 v[16:17], v[16:17], v[18:19], v[46:47]
	v_cvt_pk_bf16_f32 v14, v14, v15
	s_nop 0
	v_cvt_pk_bf16_f32 v15, v16, v17
	global_store_dwordx2 v[56:57], v[14:15], off offset:-512
	s_cbranch_scc1 .LBB0_1067
